# i5 + grid barrier: waiters poll the top-level arrival counter against its all-arrived value instead of the generation word bumped one atomic round trip later
# speedup vs baseline: 1.0026x; 1.0026x over previous
.LBB0_764:
	v_readlane_b32 s4, v243, 61
	v_readlane_b32 s5, v243, 62
	v_cvt_f32_u32_e32 v1, v4
	v_sub_u32_e32 v6, 0, v4
	v_rcp_iflag_f32_e32 v1, v1
	s_nop 1
	buffer_inv sc1
	global_atomic_add v5, v3, v216, s[4:5] sc0
	v_mul_f32_e32 v1, 0x4f7ffffe, v1
	v_cvt_u32_f32_e32 v1, v1
	v_mul_lo_u32 v6, v6, v1
	v_mul_hi_u32 v6, v1, v6
	v_add_u32_e32 v1, v1, v6
	s_waitcnt vmcnt(0)
	v_mul_hi_u32 v1, v5, v1
	v_mul_lo_u32 v6, v1, v4
	v_sub_u32_e32 v6, v5, v6
	v_add_u32_e32 v7, 1, v1
	v_cmp_ge_u32_e32 vcc, v6, v4
	v_add_u32_e32 v5, 1, v5
	s_nop 0
	v_cndmask_b32_e32 v1, v1, v7, vcc
	v_sub_u32_e32 v7, v6, v4
	v_cndmask_b32_e32 v6, v6, v7, vcc
	v_add_u32_e32 v7, 1, v1
	v_cmp_ge_u32_e32 vcc, v6, v4
	s_nop 1
	v_cndmask_b32_e32 v1, v1, v7, vcc
	v_mul_lo_u32 v6, v4, v1
	v_add_u32_e32 v4, v6, v4
	v_cmp_ne_u32_e32 vcc, v5, v4
	s_and_saveexec_b64 s[4:5], vcc
	s_xor_b64 s[4:5], exec, s[4:5]
	s_cbranch_execz .LBB0_778
	s_waitcnt lgkmcnt(0)
	v_readlane_b32 s98, v242, 1
	v_readlane_b32 s99, v242, 2
	s_nop 4
	v_mad_u32_u24 v1, v1, v2, v2
	global_load_dword v2, v3, s[98:99] offset:-256 sc1
	s_waitcnt vmcnt(0)
	v_cmp_lt_u32_e32 vcc, v2, v1
	s_and_saveexec_b64 s[6:7], vcc
	s_cbranch_execz .LBB0_777
	s_mov_b32 s19, 1
	s_mov_b64 s[8:9], 0
	s_branch .LBB0_768

.LBB0_770:
	global_load_dword v2, v3, s[98:99] offset:-256 sc1
	s_add_i32 s19, s19, 1
	s_mov_b64 s[14:15], -1
	s_waitcnt vmcnt(0)
	v_cmp_ge_u32_e32 vcc, v2, v1
	s_orn2_b64 s[12:13], vcc, exec
	s_branch .LBB0_767

.LBB0_781:
	s_or_b64 exec, exec, s[6:7]
	s_waitcnt vmcnt(0)
	v_readfirstlane_b32 s4, v4
	v_sub_u32_e32 v5, 0, v2
	s_mov_b64 s[6:7], -1
	v_add_u32_e32 v4, s4, v1
	v_cvt_f32_u32_e32 v1, v2
	v_readlane_b32 s4, v242, 1
	v_readlane_b32 s5, v242, 2
	v_rcp_iflag_f32_e32 v1, v1
	s_nop 0
	v_mul_f32_e32 v1, 0x4f7ffffe, v1
	v_cvt_u32_f32_e32 v1, v1
	v_mul_lo_u32 v5, v5, v1
	v_mul_hi_u32 v5, v1, v5
	v_add_u32_e32 v1, v1, v5
	v_mul_hi_u32 v1, v4, v1
	v_mul_lo_u32 v5, v1, v2
	v_sub_u32_e32 v5, v4, v5
	v_cmp_ge_u32_e32 vcc, v5, v2
	v_add_u32_e32 v6, 1, v1
	v_add_u32_e32 v4, 1, v4
	v_cndmask_b32_e32 v1, v1, v6, vcc
	v_sub_u32_e32 v6, v5, v2
	v_cndmask_b32_e32 v5, v5, v6, vcc
	v_cmp_ge_u32_e32 vcc, v5, v2
	v_add_u32_e32 v5, 1, v1
	s_nop 0
	v_cndmask_b32_e32 v1, v1, v5, vcc
	v_mul_lo_u32 v5, v2, v1
	v_add_u32_e32 v2, v5, v2
	v_cmp_ne_u32_e32 vcc, v4, v2
	v_mov_b64_e32 v[4:5], s[4:5]
	s_and_saveexec_b64 s[4:5], vcc
	s_cbranch_execz .LBB0_793
	v_readlane_b32 s6, v242, 1
	v_readlane_b32 s7, v242, 2
	s_mov_b64 s[8:9], 0
	s_nop 3
	v_mov_b32_e32 v1, v2
	global_load_dword v2, v3, s[6:7] offset:-256 sc1
	s_waitcnt vmcnt(0)
	v_cmp_lt_u32_e32 vcc, v2, v1
	s_and_saveexec_b64 s[6:7], vcc
	s_cbranch_execz .LBB0_792
	s_mov_b32 s19, 1
	s_branch .LBB0_785

.LBB0_787:
	v_readlane_b32 s12, v242, 1
	v_readlane_b32 s13, v242, 2
	s_add_i32 s19, s19, 1
	s_mov_b64 s[14:15], -1
	s_nop 2
	global_load_dword v2, v3, s[12:13] offset:-256 sc1
	s_waitcnt vmcnt(0)
	v_cmp_ge_u32_e32 vcc, v2, v1
	s_orn2_b64 s[12:13], vcc, exec
	s_branch .LBB0_784

.LBB0_2938:
	v_readlane_b32 s4, v243, 61
	v_readlane_b32 s5, v243, 62
	v_cvt_f32_u32_e32 v1, v4
	v_sub_u32_e32 v6, 0, v4
	v_rcp_iflag_f32_e32 v1, v1
	s_nop 1
	buffer_inv sc1
	global_atomic_add v5, v3, v216, s[4:5] sc0
	v_mul_f32_e32 v1, 0x4f7ffffe, v1
	v_cvt_u32_f32_e32 v1, v1
	v_mul_lo_u32 v6, v6, v1
	v_mul_hi_u32 v6, v1, v6
	v_add_u32_e32 v1, v1, v6
	s_waitcnt vmcnt(0)
	v_mul_hi_u32 v1, v5, v1
	v_mul_lo_u32 v6, v1, v4
	v_sub_u32_e32 v6, v5, v6
	v_add_u32_e32 v7, 1, v1
	v_cmp_ge_u32_e32 vcc, v6, v4
	v_add_u32_e32 v5, 1, v5
	s_nop 0
	v_cndmask_b32_e32 v1, v1, v7, vcc
	v_sub_u32_e32 v7, v6, v4
	v_cndmask_b32_e32 v6, v6, v7, vcc
	v_add_u32_e32 v7, 1, v1
	v_cmp_ge_u32_e32 vcc, v6, v4
	s_nop 1
	v_cndmask_b32_e32 v1, v1, v7, vcc
	v_mul_lo_u32 v6, v4, v1
	v_add_u32_e32 v4, v6, v4
	v_cmp_ne_u32_e32 vcc, v5, v4
	s_and_saveexec_b64 s[4:5], vcc
	s_xor_b64 s[4:5], exec, s[4:5]
	s_cbranch_execz .LBB0_2952
	s_waitcnt lgkmcnt(0)
	v_readlane_b32 s98, v242, 1
	v_readlane_b32 s99, v242, 2
	s_nop 4
	v_mad_u32_u24 v1, v1, v2, v2
	global_load_dword v2, v3, s[98:99] offset:-256 sc1
	s_waitcnt vmcnt(0)
	v_cmp_lt_u32_e32 vcc, v2, v1
	s_and_saveexec_b64 s[6:7], vcc
	s_cbranch_execz .LBB0_2951
	s_mov_b32 s18, 1
	s_mov_b64 s[8:9], 0
	s_branch .LBB0_2942

.LBB0_2944:
	global_load_dword v2, v3, s[98:99] offset:-256 sc1
	s_add_i32 s18, s18, 1
	s_mov_b64 s[14:15], -1
	s_waitcnt vmcnt(0)
	v_cmp_ge_u32_e32 vcc, v2, v1
	s_orn2_b64 s[12:13], vcc, exec
	s_branch .LBB0_2941

.LBB0_2955:
	s_or_b64 exec, exec, s[6:7]
	s_waitcnt vmcnt(0)
	v_readfirstlane_b32 s4, v4
	v_sub_u32_e32 v5, 0, v2
	s_mov_b64 s[6:7], -1
	v_add_u32_e32 v4, s4, v1
	v_cvt_f32_u32_e32 v1, v2
	v_readlane_b32 s4, v242, 1
	v_readlane_b32 s5, v242, 2
	v_rcp_iflag_f32_e32 v1, v1
	s_nop 0
	v_mul_f32_e32 v1, 0x4f7ffffe, v1
	v_cvt_u32_f32_e32 v1, v1
	v_mul_lo_u32 v5, v5, v1
	v_mul_hi_u32 v5, v1, v5
	v_add_u32_e32 v1, v1, v5
	v_mul_hi_u32 v1, v4, v1
	v_mul_lo_u32 v5, v1, v2
	v_sub_u32_e32 v5, v4, v5
	v_cmp_ge_u32_e32 vcc, v5, v2
	v_add_u32_e32 v6, 1, v1
	v_add_u32_e32 v4, 1, v4
	v_cndmask_b32_e32 v1, v1, v6, vcc
	v_sub_u32_e32 v6, v5, v2
	v_cndmask_b32_e32 v5, v5, v6, vcc
	v_cmp_ge_u32_e32 vcc, v5, v2
	v_add_u32_e32 v5, 1, v1
	s_nop 0
	v_cndmask_b32_e32 v1, v1, v5, vcc
	v_mul_lo_u32 v5, v2, v1
	v_add_u32_e32 v2, v5, v2
	v_cmp_ne_u32_e32 vcc, v4, v2
	v_mov_b64_e32 v[4:5], s[4:5]
	s_and_saveexec_b64 s[4:5], vcc
	s_cbranch_execz .LBB0_2967
	v_readlane_b32 s6, v242, 1
	v_readlane_b32 s7, v242, 2
	s_mov_b64 s[8:9], 0
	s_nop 3
	v_mov_b32_e32 v1, v2
	global_load_dword v2, v3, s[6:7] offset:-256 sc1
	s_waitcnt vmcnt(0)
	v_cmp_lt_u32_e32 vcc, v2, v1
	s_and_saveexec_b64 s[6:7], vcc
	s_cbranch_execz .LBB0_2966
	s_mov_b32 s18, 1
	s_branch .LBB0_2959

.LBB0_2961:
	v_readlane_b32 s12, v242, 1
	v_readlane_b32 s13, v242, 2
	s_add_i32 s18, s18, 1
	s_mov_b64 s[14:15], -1
	s_nop 2
	global_load_dword v2, v3, s[12:13] offset:-256 sc1
	s_waitcnt vmcnt(0)
	v_cmp_ge_u32_e32 vcc, v2, v1
	s_orn2_b64 s[12:13], vcc, exec
	s_branch .LBB0_2958
